# baseline (speedup 1.0000x reference)
.LBB2_25:
	s_load_dwordx2 s[36:37], s[0:1], 0x30
	s_mov_b32 s38, 0
	v_and_b32_e32 v69, 15, v0
	s_and_b64 vcc, exec, s[2:3]
	s_cbranch_vccz .LBB2_53
	v_cmp_gt_i32_e32 vcc, 32, v35
	s_cmp_lg_u64 vcc, exec
	v_cmp_lt_i32_e64 s[2:3], v69, v35
	s_cbranch_scc0 .LBB2_38
	v_mov_b32_e32 v3, 0
	v_mov_b32_e32 v6, v34
	v_mov_b32_e32 v7, 0
	v_mov_b32_e32 v8, 0
	s_and_saveexec_b64 s[4:5], s[2:3]
	s_cbranch_execz .LBB2_29
	v_add_u32_e32 v4, v36, v69
	v_ashrrev_i32_e32 v5, 31, v4
	v_lshl_add_u64 v[4:5], v[4:5], 4, s[30:31]
	global_load_dwordx4 v[6:9], v[4:5], off nt

.Ll1_r2b:
	s_mov_b64 exec, s[6:7]
	v_mov_b32_e32 v11, 0
	s_waitcnt vmcnt(0)
	v_or_b32_e32 v9, 16, v69
	v_lshlrev_b32_e32 v10, 2, v6
	v_lshl_add_u64 v[26:27], v[10:11], 2, s[28:29]
	v_lshlrev_b32_e32 v10, 2, v2
	v_lshl_add_u64 v[10:11], v[10:11], 2, s[28:29]
	global_load_dwordx3 v[22:24], v[26:27], off offset:4
	global_load_dwordx4 v[18:21], v[10:11], off
	v_lshlrev_b32_e32 v10, 2, v34
	v_ashrrev_i32_e32 v11, 31, v10
	v_lshlrev_b64 v[10:11], 2, v[10:11]
	s_waitcnt lgkmcnt(0)
	v_lshl_add_u64 v[12:13], s[34:35], 0, v[10:11]
	v_lshl_add_u64 v[10:11], s[28:29], 0, v[10:11]
	global_load_dwordx4 v[14:17], v[12:13], off
	v_cvt_f32_f16_e32 v29, v7
	global_load_dwordx4 v[10:13], v[10:11], off
	global_load_dword v25, v[26:27], off
	s_movk_i32 s8, 0x410
	v_mul_lo_u32 v70, v41, s8
	v_lshlrev_b32_e32 v71, 4, v69
	s_mov_b32 s38, 1
	v_lshl_add_u32 v47, v69, 2, v70
	ds_write2_b32 v47, v6, v2 offset0:192 offset1:208
	s_mov_b32 s21, s44
	ds_read_b96 v[62:64], v70 offset:768
	ds_read2_b32 v[66:67], v70 offset0:195 offset1:196
	ds_read_b32 v65, v70 offset:788
	s_waitcnt lgkmcnt(2)
	v_lshl_or_b32 v74, v62, 8, v71
	v_lshl_or_b32 v78, v63, 8, v71
	v_lshl_or_b32 v82, v64, 8, v71
	buffer_load_dwordx4 v[74:77], v74, s[20:23], 0 offen
	buffer_load_dwordx4 v[78:81], v78, s[20:23], 0 offen
	buffer_load_dwordx4 v[82:85], v82, s[20:23], 0 offen
	s_waitcnt lgkmcnt(0)
	v_lshl_or_b32 v86, v66, 8, v71
	v_lshl_or_b32 v90, v67, 8, v71
	v_lshl_or_b32 v50, v65, 8, v71
	buffer_load_dwordx4 v[86:89], v86, s[20:23], 0 offen
	buffer_load_dwordx4 v[90:93], v90, s[20:23], 0 offen
	buffer_load_dwordx4 v[50:53], v50, s[20:23], 0 offen
	v_mov_b32_e32 v5, 0xff800000
	v_mov_b32_e32 v28, 0xff800000
	s_and_saveexec_b64 s[6:7], s[2:3]
	s_cbranch_execz .LBB2_45
	s_waitcnt vmcnt(6)
	v_add_f32_e32 v25, v14, v25
	v_add_f32_e32 v25, v25, v29
	v_mul_f32_e32 v26, 0x3e4ccccd, v25
	v_cmp_lt_f32_e32 vcc, 0, v25
	s_nop 1
	v_cndmask_b32_e32 v28, v26, v25, vcc
.LBB2_45:
	s_or_b64 exec, exec, s[6:7]
	v_cvt_f32_i32_e32 v26, v35
	v_cvt_f32_f16_sdwa v32, v7 dst_sel:DWORD dst_unused:UNUSED_PAD src0_sel:WORD_1
	v_cvt_f32_f16_e32 v30, v3
	s_waitcnt vmcnt(6)
	v_add_f32_e32 v18, v18, v14
	v_max_f32_e32 v7, 1.0, v26
	v_div_scale_f32 v26, s[6:7], v7, v7, 1.0
	v_rcp_f32_e32 v27, v26
	v_div_scale_f32 v31, vcc, 1.0, v7, 1.0
	v_add_f32_e32 v18, v18, v30
	v_fma_f32 v33, -v26, v27, 1.0
	v_fmac_f32_e32 v27, v33, v27
	v_mul_f32_e32 v33, v31, v27
	v_fma_f32 v36, -v26, v33, v31
	v_fmac_f32_e32 v33, v36, v27
	v_fma_f32 v26, -v26, v33, v31
	v_div_fmas_f32 v26, v26, v27, v33
	v_div_fixup_f32 v7, v26, v7, 1.0
	v_add_f32_e32 v26, 0, v29
	v_mul_f32_e32 v27, 0x3e4ccccd, v18
	v_cmp_lt_f32_e32 vcc, 0, v18
	v_cndmask_b32_e64 v26, 0, v26, s[2:3]
	s_mov_b32 s10, 0xff800000
	v_cndmask_b32_e32 v18, v27, v18, vcc
	v_cndmask_b32_e64 v27, 0, v30, s[4:5]
	v_add_f32_e32 v26, v26, v27
	s_waitcnt vmcnt(6)
	v_mov_b32_e32 v30, v10
	v_cndmask_b32_e64 v18, v5, v18, s[4:5]
	v_add_f32_dpp v26, v26, v26 quad_perm:[1,0,3,2] row_mask:0xf bank_mask:0xf
	v_max3_f32 v29, v28, s10, v18
	v_cvt_f32_f16_e32 v25, v8
	v_add_f32_dpp v26, v26, v26 quad_perm:[2,3,0,1] row_mask:0xf bank_mask:0xf
	v_add_f32_e32 v19, v19, v15
	v_lshlrev_b32_e32 v71, 4, v69
	v_add_f32_dpp v27, v26, v26 row_half_mirror row_mask:0xf bank_mask:0xf
	v_mov_b32_e32 v31, v27
	v_mov_b32_e32 v26, v14
	s_nop 0
	v_mov_b32_dpp v31, v31 row_mirror row_mask:0xf bank_mask:0xf
	v_pk_add_f32 v[26:27], v[26:27], v[30:31]
	s_nop 0
	v_fmac_f32_e32 v26, v7, v27
	v_mul_f32_e32 v10, 0x3e4ccccd, v26
	v_cmp_lt_f32_e32 vcc, 0, v26
	s_nop 1
	v_cndmask_b32_e32 v14, v10, v26, vcc
	v_cmp_eq_u32_e32 vcc, v69, v35
	s_nop 0
	v_max_f32_dpp v10, v29, v29 quad_perm:[1,0,3,2] row_mask:0xf bank_mask:0xf
	v_cvt_f32_f16_e32 v29, v4
	s_nop 0
	v_max_f32_dpp v10, v10, v10 quad_perm:[2,3,0,1] row_mask:0xf bank_mask:0xf
	s_nop 1
	v_max_f32_dpp v10, v10, v10 row_half_mirror row_mask:0xf bank_mask:0xf
	s_nop 1
	v_max_f32_dpp v26, v10, v10 row_mirror row_mask:0xf bank_mask:0xf
	v_max_f32_e32 v26, v26, v14
	v_sub_f32_e32 v10, v28, v26
	v_mul_f32_e32 v10, 0x3fb8aa3b, v10
	v_exp_f32_e32 v27, v10
	v_sub_f32_e32 v10, v18, v26
	v_mul_f32_e32 v10, 0x3fb8aa3b, v10
	v_exp_f32_e32 v28, v10
	v_cvt_f32_f16_sdwa v10, v8 dst_sel:DWORD dst_unused:UNUSED_PAD src0_sel:WORD_1
	v_add_f32_e32 v8, 0, v27
	v_cndmask_b32_e64 v8, 0, v8, s[2:3]
	v_cndmask_b32_e64 v18, 0, v28, s[4:5]
	v_add_f32_e32 v8, v18, v8
	v_sub_f32_e32 v14, v14, v26
	v_mul_f32_e32 v14, 0x3fb8aa3b, v14
	v_add_f32_dpp v8, v8, v8 quad_perm:[1,0,3,2] row_mask:0xf bank_mask:0xf
	v_exp_f32_e32 v14, v14
	s_nop 0
	v_add_f32_dpp v8, v8, v8 quad_perm:[2,3,0,1] row_mask:0xf bank_mask:0xf
	s_nop 1
	v_add_f32_dpp v8, v8, v8 row_half_mirror row_mask:0xf bank_mask:0xf
	s_nop 1
	v_add_f32_dpp v8, v8, v8 row_mirror row_mask:0xf bank_mask:0xf
	v_add_f32_e32 v8, v14, v8
	v_add_f32_e32 v8, 0x24e69595, v8
	v_rcp_f32_e32 v26, v8
	v_cvt_f32_f16_sdwa v18, v3 dst_sel:DWORD dst_unused:UNUSED_PAD src0_sel:WORD_1
	v_cvt_f32_f16_sdwa v3, v4 dst_sel:DWORD dst_unused:UNUSED_PAD src0_sel:WORD_1
	v_mul_f32_e32 v4, v14, v26
	v_mul_f32_e32 v8, v27, v26
	v_cndmask_b32_e32 v14, 0, v4, vcc
	v_cndmask_b32_e64 v8, v14, v8, s[2:3]
	v_add_f32_e32 v14, v22, v15
	v_add_f32_e32 v14, v14, v32
	v_mul_f32_e32 v22, 0x3e4ccccd, v14
	v_cmp_lt_f32_e64 s[6:7], 0, v14
	v_add_f32_e32 v19, v19, v18
	v_cndmask_b32_e64 v18, 0, v18, s[4:5]
	v_cndmask_b32_e64 v14, v22, v14, s[6:7]
	v_cndmask_b32_e64 v22, v5, v14, s[2:3]
	v_add_f32_e32 v14, 0, v32
	v_cndmask_b32_e64 v14, 0, v14, s[2:3]
	v_add_f32_e32 v14, v14, v18
	v_mul_f32_e32 v27, 0x3e4ccccd, v19
	v_cmp_lt_f32_e64 s[6:7], 0, v19
	v_add_f32_dpp v14, v14, v14 quad_perm:[1,0,3,2] row_mask:0xf bank_mask:0xf
	s_nop 0
	v_cndmask_b32_e64 v19, v27, v19, s[6:7]
	v_cndmask_b32_e64 v27, v5, v19, s[4:5]
	v_add_f32_dpp v14, v14, v14 quad_perm:[2,3,0,1] row_mask:0xf bank_mask:0xf
	v_max3_f32 v30, v22, s10, v27
	s_nop 0
	v_add_f32_dpp v19, v14, v14 row_half_mirror row_mask:0xf bank_mask:0xf
	v_mov_b32_e32 v18, v15
	v_mov_b32_e32 v15, v19
	v_mov_b32_e32 v14, v11
	s_nop 0
	v_mov_b32_dpp v15, v15 row_mirror row_mask:0xf bank_mask:0xf
	v_pk_add_f32 v[14:15], v[18:19], v[14:15]
	s_nop 0
	v_fmac_f32_e32 v14, v7, v15
	v_mul_f32_e32 v11, 0x3e4ccccd, v14
	v_cmp_lt_f32_e64 s[6:7], 0, v14
	s_nop 1
	v_cndmask_b32_e64 v11, v11, v14, s[6:7]
	v_cmp_eq_u32_e64 s[6:7], v9, v35
	s_nop 0
	v_max_f32_dpp v14, v30, v30 quad_perm:[1,0,3,2] row_mask:0xf bank_mask:0xf
	v_cndmask_b32_e64 v4, 0, v4, s[6:7]
	s_nop 0
	v_max_f32_dpp v14, v14, v14 quad_perm:[2,3,0,1] row_mask:0xf bank_mask:0xf
	s_nop 1
	v_max_f32_dpp v14, v14, v14 row_half_mirror row_mask:0xf bank_mask:0xf
	s_nop 1
	v_max_f32_dpp v15, v14, v14 row_mirror row_mask:0xf bank_mask:0xf
	v_max_f32_e32 v14, v15, v11
	v_sub_f32_e32 v15, v22, v14
	v_mul_f32_e32 v15, 0x3fb8aa3b, v15
	v_sub_f32_e32 v18, v27, v14
	v_exp_f32_e32 v15, v15
	v_mul_f32_e32 v18, 0x3fb8aa3b, v18
	v_exp_f32_e32 v27, v18
	v_sub_f32_e32 v11, v11, v14
	v_add_f32_e32 v19, 0, v15
	v_cndmask_b32_e64 v19, 0, v19, s[2:3]
	v_cndmask_b32_e64 v22, 0, v27, s[4:5]
	v_add_f32_e32 v19, v22, v19
	v_mul_f32_e32 v11, 0x3fb8aa3b, v11
	v_exp_f32_e32 v11, v11
	v_add_f32_dpp v14, v19, v19 quad_perm:[1,0,3,2] row_mask:0xf bank_mask:0xf
	v_mul_f32_e32 v18, v28, v26
	v_mov_b32_e32 v22, v12
	v_add_f32_dpp v14, v14, v14 quad_perm:[2,3,0,1] row_mask:0xf bank_mask:0xf
	s_nop 1
	v_add_f32_dpp v14, v14, v14 row_half_mirror row_mask:0xf bank_mask:0xf
	s_nop 1
	v_add_f32_dpp v14, v14, v14 row_mirror row_mask:0xf bank_mask:0xf
	v_add_f32_e32 v14, v11, v14
	v_add_f32_e32 v14, 0x24e69595, v14
	v_rcp_f32_e32 v26, v14
	v_add_f32_e32 v19, v20, v16
	v_cndmask_b32_e64 v14, v4, v18, s[4:5]
	v_add_f32_e32 v19, v19, v29
	v_mul_f32_e32 v9, v15, v26
	v_add_f32_e32 v15, v23, v16
	v_add_f32_e32 v15, v15, v25
	v_mul_f32_e32 v18, 0x3e4ccccd, v15
	v_cmp_lt_f32_e64 s[8:9], 0, v15
	v_mul_f32_e32 v20, 0x3e4ccccd, v19
	v_mul_f32_e32 v4, v11, v26
	v_cndmask_b32_e64 v15, v18, v15, s[8:9]
	v_add_f32_e32 v18, 0, v25
	v_cmp_lt_f32_e64 s[8:9], 0, v19
	v_cndmask_b32_e64 v18, 0, v18, s[2:3]
	v_cndmask_b32_e64 v15, v5, v15, s[2:3]
	v_cndmask_b32_e64 v19, v20, v19, s[8:9]
	v_cndmask_b32_e64 v20, 0, v29, s[4:5]
	v_add_f32_e32 v18, v18, v20
	v_cndmask_b32_e64 v25, v5, v19, s[4:5]
	v_max3_f32 v28, v15, s10, v25
	v_cndmask_b32_e32 v11, 0, v4, vcc
	v_add_f32_dpp v18, v18, v18 quad_perm:[1,0,3,2] row_mask:0xf bank_mask:0xf
	v_cndmask_b32_e64 v9, v11, v9, s[2:3]
	v_cndmask_b32_e64 v4, 0, v4, s[6:7]
	v_add_f32_dpp v18, v18, v18 quad_perm:[2,3,0,1] row_mask:0xf bank_mask:0xf
	s_nop 1
	v_add_f32_dpp v19, v18, v18 row_half_mirror row_mask:0xf bank_mask:0xf
	v_mov_b32_e32 v23, v19
	v_mov_b32_e32 v18, v16
	s_nop 0
	v_mov_b32_dpp v23, v23 row_mirror row_mask:0xf bank_mask:0xf
	v_pk_add_f32 v[18:19], v[18:19], v[22:23]
	v_fmac_f32_e32 v18, v7, v19
	v_mul_f32_e32 v12, 0x3e4ccccd, v18
	v_cmp_lt_f32_e64 s[8:9], 0, v18
	v_max_f32_dpp v16, v28, v28 quad_perm:[1,0,3,2] row_mask:0xf bank_mask:0xf
	s_nop 0
	v_cndmask_b32_e64 v12, v12, v18, s[8:9]
	s_nop 1
	v_max_f32_dpp v16, v16, v16 quad_perm:[2,3,0,1] row_mask:0xf bank_mask:0xf
	s_nop 1
	v_max_f32_dpp v16, v16, v16 row_half_mirror row_mask:0xf bank_mask:0xf
	s_nop 1
	v_max_f32_dpp v18, v16, v16 row_mirror row_mask:0xf bank_mask:0xf
	v_max_f32_e32 v16, v18, v12
	v_sub_f32_e32 v15, v15, v16
	v_mul_f32_e32 v15, 0x3fb8aa3b, v15
	v_exp_f32_e32 v18, v15
	v_sub_f32_e32 v15, v25, v16
	v_mul_f32_e32 v15, 0x3fb8aa3b, v15
	v_exp_f32_e32 v19, v15
	v_add_f32_e32 v11, 0, v18
	v_cndmask_b32_e64 v11, 0, v11, s[2:3]
	v_sub_f32_e32 v12, v12, v16
	v_cndmask_b32_e64 v15, 0, v19, s[4:5]
	v_add_f32_e32 v11, v15, v11
	v_mul_f32_e32 v12, 0x3fb8aa3b, v12
	v_exp_f32_e32 v12, v12
	v_add_f32_dpp v11, v11, v11 quad_perm:[1,0,3,2] row_mask:0xf bank_mask:0xf
	s_nop 1
	v_add_f32_dpp v11, v11, v11 quad_perm:[2,3,0,1] row_mask:0xf bank_mask:0xf
	s_nop 1
	v_add_f32_dpp v11, v11, v11 row_half_mirror row_mask:0xf bank_mask:0xf
	s_nop 1
	v_add_f32_dpp v11, v11, v11 row_mirror row_mask:0xf bank_mask:0xf
	v_add_f32_e32 v11, v12, v11
	v_add_f32_e32 v11, 0x24e69595, v11
	v_rcp_f32_e32 v16, v11
	v_mul_f32_e32 v11, v27, v26
	v_cndmask_b32_e64 v15, v4, v11, s[4:5]
	v_add_f32_e32 v4, v24, v17
	v_add_f32_e32 v4, v4, v10
	v_mul_f32_e32 v11, 0x3e4ccccd, v4
	v_cmp_lt_f32_e64 s[8:9], 0, v4
	v_mul_f32_e32 v12, v12, v16
	v_cndmask_b32_e32 v20, 0, v12, vcc
	v_cndmask_b32_e64 v4, v11, v4, s[8:9]
	v_cndmask_b32_e64 v22, v5, v4, s[2:3]
	v_add_f32_e32 v4, 0, v10
	v_add_f32_e32 v10, v21, v17
	v_cndmask_b32_e64 v4, 0, v4, s[2:3]
	v_add_f32_e32 v10, v10, v3
	v_cndmask_b32_e64 v3, 0, v3, s[4:5]
	v_add_f32_e32 v3, v4, v3
	v_mul_f32_e32 v11, 0x3e4ccccd, v10
	v_cmp_lt_f32_e64 s[8:9], 0, v10
	v_add_f32_dpp v3, v3, v3 quad_perm:[1,0,3,2] row_mask:0xf bank_mask:0xf
	s_nop 0
	v_cndmask_b32_e64 v10, v11, v10, s[8:9]
	v_cndmask_b32_e64 v21, v5, v10, s[4:5]
	v_add_f32_dpp v3, v3, v3 quad_perm:[2,3,0,1] row_mask:0xf bank_mask:0xf
	v_mov_b32_e32 v10, v13
	v_max3_f32 v23, v22, s10, v21
	v_add_f32_dpp v5, v3, v3 row_half_mirror row_mask:0xf bank_mask:0xf
	v_mov_b32_e32 v11, v5
	v_mov_b32_e32 v4, v17
	v_cndmask_b32_e64 v12, 0, v12, s[6:7]
	v_mov_b32_dpp v11, v11 row_mirror row_mask:0xf bank_mask:0xf
	v_pk_add_f32 v[4:5], v[4:5], v[10:11]
	v_mul_f32_e32 v18, v18, v16
	v_fmac_f32_e32 v4, v7, v5
	v_mul_f32_e32 v3, 0x3e4ccccd, v4
	v_cmp_lt_f32_e64 s[8:9], 0, v4
	v_cndmask_b32_e64 v10, v20, v18, s[2:3]
	s_nop 0
	v_cndmask_b32_e64 v3, v3, v4, s[8:9]
	s_nop 1
	v_max_f32_dpp v4, v23, v23 quad_perm:[1,0,3,2] row_mask:0xf bank_mask:0xf
	s_nop 1
	v_max_f32_dpp v4, v4, v4 quad_perm:[2,3,0,1] row_mask:0xf bank_mask:0xf
	s_nop 1
	v_max_f32_dpp v4, v4, v4 row_half_mirror row_mask:0xf bank_mask:0xf
	s_nop 1
	v_max_f32_dpp v5, v4, v4 row_mirror row_mask:0xf bank_mask:0xf
	v_max_f32_e32 v4, v5, v3
	v_sub_f32_e32 v5, v22, v4
	v_mul_f32_e32 v5, 0x3fb8aa3b, v5
	v_sub_f32_e32 v7, v21, v4
	v_exp_f32_e32 v5, v5
	v_mul_f32_e32 v7, 0x3fb8aa3b, v7
	v_exp_f32_e32 v7, v7
	v_sub_f32_e32 v3, v3, v4
	v_add_f32_e32 v11, 0, v5
	v_cndmask_b32_e64 v11, 0, v11, s[2:3]
	v_cndmask_b32_e64 v13, 0, v7, s[4:5]
	v_add_f32_e32 v11, v13, v11
	v_mul_f32_e32 v3, 0x3fb8aa3b, v3
	v_exp_f32_e32 v3, v3
	v_add_f32_dpp v4, v11, v11 quad_perm:[1,0,3,2] row_mask:0xf bank_mask:0xf
	s_nop 1
	v_add_f32_dpp v4, v4, v4 quad_perm:[2,3,0,1] row_mask:0xf bank_mask:0xf
	s_nop 1
	v_add_f32_dpp v4, v4, v4 row_half_mirror row_mask:0xf bank_mask:0xf
	s_nop 1
	v_add_f32_dpp v4, v4, v4 row_mirror row_mask:0xf bank_mask:0xf
	v_add_f32_e32 v4, v3, v4
	v_add_f32_e32 v4, 0x24e69595, v4
	v_rcp_f32_e32 v4, v4
	v_mul_f32_e32 v11, v19, v16
	v_cndmask_b32_e64 v16, v12, v11, s[4:5]
	v_mul_f32_e32 v3, v3, v4
	v_mul_f32_e32 v5, v5, v4
	v_cndmask_b32_e32 v11, 0, v3, vcc
	v_cndmask_b32_e64 v11, v11, v5, s[2:3]
	v_mul_f32_e32 v4, v7, v4
	v_cndmask_b32_e64 v3, 0, v3, s[6:7]
	s_movk_i32 s2, 0x410
	v_cndmask_b32_e64 v17, v3, v4, s[4:5]
	v_mul_lo_u32 v70, v41, s2
	v_lshlrev_b32_e32 v4, 2, v69
	v_add_u32_e32 v3, v70, v71
	v_add_u32_e32 v4, v70, v4
	v_cmp_gt_u32_e32 vcc, 2, v69
	ds_write_b128 v3, v[8:11]
	ds_write_b128 v3, v[14:17] offset:256
	ds_write2_b32 v4, v6, v2 offset0:192 offset1:208
	s_and_saveexec_b64 s[2:3], vcc
	s_cbranch_execz .LBB2_47
	v_mov_b32_e32 v6, 0
	v_mov_b32_e32 v7, v6
	v_mov_b32_e32 v8, v6
	v_mov_b32_e32 v9, v6
	ds_write_b128 v3, v[6:9] offset:512
	ds_write_b32 v4, v34 offset:896

.LBB2_48:
	v_readlane_b32 s2, v35, 0
	v_readlane_b32 s3, v35, 16
	s_max_i32 s2, s2, s3
	v_readlane_b32 s3, v35, 32
	v_readlane_b32 s4, v35, 48
	s_nop 0
	v_mov_b32_e32 v2, s3
	v_mov_b32_e32 v3, s4
	v_max3_i32 v2, s2, v2, v3
	s_mov_b32 s2, 3
	v_readfirstlane_b32 s3, v2
	s_add_i32 s3, s3, 3
	s_mul_hi_i32 s3, s3, 0x55555556
	s_lshr_b32 s4, s3, 31
	s_add_i32 s3, s3, s4
	s_mul_i32 s3, s3, 3
	s_setprio 3
	s_mov_b32 s21, s44
	s_cmp_eq_u32 s38, 1
	s_cbranch_scc1 .Ll1g_pre2
	ds_read_b96 v[62:64], v70 offset:768
	s_cmp_gt_i32 s3, 3
	s_cselect_b32 s4, 12, 0
	v_add_u32_e32 v73, s4, v70
	ds_read2_b32 v[66:67], v73 offset0:192 offset1:193
	ds_read_b32 v65, v73 offset:776
	s_waitcnt lgkmcnt(2)
	v_lshl_or_b32 v74, v62, 8, v71
	v_lshl_or_b32 v78, v63, 8, v71
	v_lshl_or_b32 v82, v64, 8, v71
	buffer_load_dwordx4 v[74:77], v74, s[20:23], 0 offen
	buffer_load_dwordx4 v[78:81], v78, s[20:23], 0 offen
	buffer_load_dwordx4 v[82:85], v82, s[20:23], 0 offen
	s_waitcnt lgkmcnt(0)
	v_lshl_or_b32 v86, v66, 8, v71
	v_lshl_or_b32 v90, v67, 8, v71
	v_lshl_or_b32 v50, v65, 8, v71
	buffer_load_dwordx4 v[86:89], v86, s[20:23], 0 offen
	buffer_load_dwordx4 v[90:93], v90, s[20:23], 0 offen
	buffer_load_dwordx4 v[50:53], v50, s[20:23], 0 offen
.Ll1g_pre2:
	v_mov_b32_e32 v18, 0
	v_mov_b32_e32 v19, v18
	v_mov_b32_e32 v20, v18
	v_mov_b32_e32 v21, v18
	v_mov_b32_e32 v22, v18
	v_mov_b32_e32 v23, v18
	v_mov_b32_e32 v24, v18
	v_mov_b32_e32 v25, v18
	v_mov_b32_e32 v26, v18
	v_mov_b32_e32 v27, v18
	v_mov_b32_e32 v28, v18
	v_mov_b32_e32 v29, v18
	v_mov_b32_e32 v30, v18
	v_mov_b32_e32 v31, v18
	v_mov_b32_e32 v32, v18
	v_mov_b32_e32 v33, v18
	v_mov_b32_e32 v34, v18
	v_mov_b32_e32 v35, v18
	v_mov_b32_e32 v36, v18
	v_mov_b32_e32 v37, v18
	v_mov_b32_e32 v38, v18
	v_mov_b32_e32 v39, v18
	v_mov_b32_e32 v40, v18
	v_mov_b32_e32 v41, v18
	v_mov_b32_e32 v42, v18
	v_mov_b32_e32 v43, v18
	v_mov_b32_e32 v44, v18
	v_mov_b32_e32 v45, v18
	v_mov_b32_e32 v46, v18
	v_mov_b32_e32 v47, v18
	v_mov_b32_e32 v48, v18
	v_mov_b32_e32 v49, v18
	v_and_b32_e32 v72, 3, v68
	v_lshl_add_u32 v72, v72, 2, v70
	s_mov_b32 s2, 0
.Ll1g_loopE:
	s_add_i32 s5, s2, 6
	s_cmp_ge_i32 s5, s3
	s_cbranch_scc1 .Ll1g_tailE
	ds_read_b32 v66, v72
	ds_read_b32 v67, v72 offset:16
	ds_read_b32 v65, v72 offset:32
	s_lshl_b32 s4, s5, 2
	v_add_u32_e32 v73, s4, v70
	ds_read2_b32 v[62:63], v73 offset0:192 offset1:193
	ds_read_b32 v64, v73 offset:776
	s_waitcnt vmcnt(3)
	v_cvt_f32_f16_sdwa v3, v74 dst_sel:DWORD dst_unused:UNUSED_PAD src0_sel:WORD_1
	v_cvt_f32_f16_e32 v2, v74
	v_cvt_f32_f16_sdwa v5, v75 dst_sel:DWORD dst_unused:UNUSED_PAD src0_sel:WORD_1
	v_cvt_f32_f16_e32 v4, v75
	v_cvt_f32_f16_sdwa v7, v76 dst_sel:DWORD dst_unused:UNUSED_PAD src0_sel:WORD_1
	v_cvt_f32_f16_e32 v6, v76
	v_cvt_f32_f16_sdwa v9, v77 dst_sel:DWORD dst_unused:UNUSED_PAD src0_sel:WORD_1
	v_cvt_f32_f16_e32 v8, v77
	v_cvt_f32_f16_sdwa v11, v78 dst_sel:DWORD dst_unused:UNUSED_PAD src0_sel:WORD_1
	v_cvt_f32_f16_e32 v10, v78
	v_cvt_f32_f16_sdwa v13, v79 dst_sel:DWORD dst_unused:UNUSED_PAD src0_sel:WORD_1
	v_cvt_f32_f16_e32 v12, v79
	v_cvt_f32_f16_sdwa v15, v80 dst_sel:DWORD dst_unused:UNUSED_PAD src0_sel:WORD_1
	v_cvt_f32_f16_e32 v14, v80
	v_cvt_f32_f16_sdwa v17, v81 dst_sel:DWORD dst_unused:UNUSED_PAD src0_sel:WORD_1
	v_cvt_f32_f16_e32 v16, v81
	s_waitcnt lgkmcnt(2)
	v_mfma_f32_4x4x1_16b_f32 v[18:21], v66, v2, v[18:21]
	v_mfma_f32_4x4x1_16b_f32 v[22:25], v66, v3, v[22:25]
	v_mfma_f32_4x4x1_16b_f32 v[26:29], v66, v4, v[26:29]
	v_mfma_f32_4x4x1_16b_f32 v[30:33], v66, v5, v[30:33]
	v_mfma_f32_4x4x1_16b_f32 v[34:37], v66, v6, v[34:37]
	v_mfma_f32_4x4x1_16b_f32 v[38:41], v66, v7, v[38:41]
	v_mfma_f32_4x4x1_16b_f32 v[42:45], v66, v8, v[42:45]
	v_mfma_f32_4x4x1_16b_f32 v[46:49], v66, v9, v[46:49]
	v_cvt_f32_f16_sdwa v55, v82 dst_sel:DWORD dst_unused:UNUSED_PAD src0_sel:WORD_1
	v_cvt_f32_f16_e32 v54, v82
	v_cvt_f32_f16_sdwa v57, v83 dst_sel:DWORD dst_unused:UNUSED_PAD src0_sel:WORD_1
	v_cvt_f32_f16_e32 v56, v83
	v_cvt_f32_f16_sdwa v59, v84 dst_sel:DWORD dst_unused:UNUSED_PAD src0_sel:WORD_1
	v_cvt_f32_f16_e32 v58, v84
	v_cvt_f32_f16_sdwa v61, v85 dst_sel:DWORD dst_unused:UNUSED_PAD src0_sel:WORD_1
	v_cvt_f32_f16_e32 v60, v85
	s_waitcnt lgkmcnt(0)
	v_lshl_or_b32 v74, v62, 8, v71
	v_lshl_or_b32 v78, v63, 8, v71
	v_lshl_or_b32 v82, v64, 8, v71
	buffer_load_dwordx4 v[74:77], v74, s[20:23], 0 offen
	buffer_load_dwordx4 v[78:81], v78, s[20:23], 0 offen
	buffer_load_dwordx4 v[82:85], v82, s[20:23], 0 offen
	v_mfma_f32_4x4x1_16b_f32 v[18:21], v67, v10, v[18:21]
	v_mfma_f32_4x4x1_16b_f32 v[22:25], v67, v11, v[22:25]
	v_mfma_f32_4x4x1_16b_f32 v[26:29], v67, v12, v[26:29]
	v_mfma_f32_4x4x1_16b_f32 v[30:33], v67, v13, v[30:33]
	v_mfma_f32_4x4x1_16b_f32 v[34:37], v67, v14, v[34:37]
	v_mfma_f32_4x4x1_16b_f32 v[38:41], v67, v15, v[38:41]
	v_mfma_f32_4x4x1_16b_f32 v[42:45], v67, v16, v[42:45]
	v_mfma_f32_4x4x1_16b_f32 v[46:49], v67, v17, v[46:49]
	v_mfma_f32_4x4x1_16b_f32 v[18:21], v65, v54, v[18:21]
	v_mfma_f32_4x4x1_16b_f32 v[22:25], v65, v55, v[22:25]
	v_mfma_f32_4x4x1_16b_f32 v[26:29], v65, v56, v[26:29]
	v_mfma_f32_4x4x1_16b_f32 v[30:33], v65, v57, v[30:33]
	v_mfma_f32_4x4x1_16b_f32 v[34:37], v65, v58, v[34:37]
	v_mfma_f32_4x4x1_16b_f32 v[38:41], v65, v59, v[38:41]
	v_mfma_f32_4x4x1_16b_f32 v[42:45], v65, v60, v[42:45]
	v_mfma_f32_4x4x1_16b_f32 v[46:49], v65, v61, v[46:49]
	v_add_u32_e32 v72, 48, v72
	s_add_i32 s2, s2, 3
.Ll1g_loopO:
	s_add_i32 s5, s2, 6
	s_cmp_ge_i32 s5, s3
	s_cbranch_scc1 .Ll1g_tailO
	ds_read_b32 v66, v72
	ds_read_b32 v67, v72 offset:16
	ds_read_b32 v65, v72 offset:32
	s_lshl_b32 s4, s5, 2
	v_add_u32_e32 v73, s4, v70
	ds_read2_b32 v[62:63], v73 offset0:192 offset1:193
	ds_read_b32 v64, v73 offset:776
	s_waitcnt vmcnt(3)
	v_cvt_f32_f16_sdwa v3, v86 dst_sel:DWORD dst_unused:UNUSED_PAD src0_sel:WORD_1
	v_cvt_f32_f16_e32 v2, v86
	v_cvt_f32_f16_sdwa v5, v87 dst_sel:DWORD dst_unused:UNUSED_PAD src0_sel:WORD_1
	v_cvt_f32_f16_e32 v4, v87
	v_cvt_f32_f16_sdwa v7, v88 dst_sel:DWORD dst_unused:UNUSED_PAD src0_sel:WORD_1
	v_cvt_f32_f16_e32 v6, v88
	v_cvt_f32_f16_sdwa v9, v89 dst_sel:DWORD dst_unused:UNUSED_PAD src0_sel:WORD_1
	v_cvt_f32_f16_e32 v8, v89
	v_cvt_f32_f16_sdwa v11, v90 dst_sel:DWORD dst_unused:UNUSED_PAD src0_sel:WORD_1
	v_cvt_f32_f16_e32 v10, v90
	v_cvt_f32_f16_sdwa v13, v91 dst_sel:DWORD dst_unused:UNUSED_PAD src0_sel:WORD_1
	v_cvt_f32_f16_e32 v12, v91
	v_cvt_f32_f16_sdwa v15, v92 dst_sel:DWORD dst_unused:UNUSED_PAD src0_sel:WORD_1
	v_cvt_f32_f16_e32 v14, v92
	v_cvt_f32_f16_sdwa v17, v93 dst_sel:DWORD dst_unused:UNUSED_PAD src0_sel:WORD_1
	v_cvt_f32_f16_e32 v16, v93
	s_waitcnt lgkmcnt(2)
	v_mfma_f32_4x4x1_16b_f32 v[18:21], v66, v2, v[18:21]
	v_mfma_f32_4x4x1_16b_f32 v[22:25], v66, v3, v[22:25]
	v_mfma_f32_4x4x1_16b_f32 v[26:29], v66, v4, v[26:29]
	v_mfma_f32_4x4x1_16b_f32 v[30:33], v66, v5, v[30:33]
	v_mfma_f32_4x4x1_16b_f32 v[34:37], v66, v6, v[34:37]
	v_mfma_f32_4x4x1_16b_f32 v[38:41], v66, v7, v[38:41]
	v_mfma_f32_4x4x1_16b_f32 v[42:45], v66, v8, v[42:45]
	v_mfma_f32_4x4x1_16b_f32 v[46:49], v66, v9, v[46:49]
	v_cvt_f32_f16_sdwa v55, v50 dst_sel:DWORD dst_unused:UNUSED_PAD src0_sel:WORD_1
	v_cvt_f32_f16_e32 v54, v50
	v_cvt_f32_f16_sdwa v57, v51 dst_sel:DWORD dst_unused:UNUSED_PAD src0_sel:WORD_1
	v_cvt_f32_f16_e32 v56, v51
	v_cvt_f32_f16_sdwa v59, v52 dst_sel:DWORD dst_unused:UNUSED_PAD src0_sel:WORD_1
	v_cvt_f32_f16_e32 v58, v52
	v_cvt_f32_f16_sdwa v61, v53 dst_sel:DWORD dst_unused:UNUSED_PAD src0_sel:WORD_1
	v_cvt_f32_f16_e32 v60, v53
	s_waitcnt lgkmcnt(0)
	v_lshl_or_b32 v86, v62, 8, v71
	v_lshl_or_b32 v90, v63, 8, v71
	v_lshl_or_b32 v50, v64, 8, v71
	buffer_load_dwordx4 v[86:89], v86, s[20:23], 0 offen
	buffer_load_dwordx4 v[90:93], v90, s[20:23], 0 offen
	buffer_load_dwordx4 v[50:53], v50, s[20:23], 0 offen
	v_mfma_f32_4x4x1_16b_f32 v[18:21], v67, v10, v[18:21]
	v_mfma_f32_4x4x1_16b_f32 v[22:25], v67, v11, v[22:25]
	v_mfma_f32_4x4x1_16b_f32 v[26:29], v67, v12, v[26:29]
	v_mfma_f32_4x4x1_16b_f32 v[30:33], v67, v13, v[30:33]
	v_mfma_f32_4x4x1_16b_f32 v[34:37], v67, v14, v[34:37]
	v_mfma_f32_4x4x1_16b_f32 v[38:41], v67, v15, v[38:41]
	v_mfma_f32_4x4x1_16b_f32 v[42:45], v67, v16, v[42:45]
	v_mfma_f32_4x4x1_16b_f32 v[46:49], v67, v17, v[46:49]
	v_mfma_f32_4x4x1_16b_f32 v[18:21], v65, v54, v[18:21]
	v_mfma_f32_4x4x1_16b_f32 v[22:25], v65, v55, v[22:25]
	v_mfma_f32_4x4x1_16b_f32 v[26:29], v65, v56, v[26:29]
	v_mfma_f32_4x4x1_16b_f32 v[30:33], v65, v57, v[30:33]
	v_mfma_f32_4x4x1_16b_f32 v[34:37], v65, v58, v[34:37]
	v_mfma_f32_4x4x1_16b_f32 v[38:41], v65, v59, v[38:41]
	v_mfma_f32_4x4x1_16b_f32 v[42:45], v65, v60, v[42:45]
	v_mfma_f32_4x4x1_16b_f32 v[46:49], v65, v61, v[46:49]
	v_add_u32_e32 v72, 48, v72
	s_add_i32 s2, s2, 3
	s_branch .Ll1g_loopE
.Ll1g_tailE:
	s_add_i32 s5, s2, 3
	s_cmp_ge_i32 s5, s3
	s_cbranch_scc1 .Ll1g_lastE
	ds_read_b32 v66, v72
	ds_read_b32 v67, v72 offset:16
	ds_read_b32 v65, v72 offset:32
	s_waitcnt vmcnt(3)
	v_cvt_f32_f16_sdwa v3, v74 dst_sel:DWORD dst_unused:UNUSED_PAD src0_sel:WORD_1
	v_cvt_f32_f16_e32 v2, v74
	v_cvt_f32_f16_sdwa v5, v75 dst_sel:DWORD dst_unused:UNUSED_PAD src0_sel:WORD_1
	v_cvt_f32_f16_e32 v4, v75
	v_cvt_f32_f16_sdwa v7, v76 dst_sel:DWORD dst_unused:UNUSED_PAD src0_sel:WORD_1
	v_cvt_f32_f16_e32 v6, v76
	v_cvt_f32_f16_sdwa v9, v77 dst_sel:DWORD dst_unused:UNUSED_PAD src0_sel:WORD_1
	v_cvt_f32_f16_e32 v8, v77
	v_cvt_f32_f16_sdwa v11, v78 dst_sel:DWORD dst_unused:UNUSED_PAD src0_sel:WORD_1
	v_cvt_f32_f16_e32 v10, v78
	v_cvt_f32_f16_sdwa v13, v79 dst_sel:DWORD dst_unused:UNUSED_PAD src0_sel:WORD_1
	v_cvt_f32_f16_e32 v12, v79
	v_cvt_f32_f16_sdwa v15, v80 dst_sel:DWORD dst_unused:UNUSED_PAD src0_sel:WORD_1
	v_cvt_f32_f16_e32 v14, v80
	v_cvt_f32_f16_sdwa v17, v81 dst_sel:DWORD dst_unused:UNUSED_PAD src0_sel:WORD_1
	v_cvt_f32_f16_e32 v16, v81
	s_waitcnt lgkmcnt(0)
	v_mfma_f32_4x4x1_16b_f32 v[18:21], v66, v2, v[18:21]
	v_mfma_f32_4x4x1_16b_f32 v[22:25], v66, v3, v[22:25]
	v_mfma_f32_4x4x1_16b_f32 v[26:29], v66, v4, v[26:29]
	v_mfma_f32_4x4x1_16b_f32 v[30:33], v66, v5, v[30:33]
	v_mfma_f32_4x4x1_16b_f32 v[34:37], v66, v6, v[34:37]
	v_mfma_f32_4x4x1_16b_f32 v[38:41], v66, v7, v[38:41]
	v_mfma_f32_4x4x1_16b_f32 v[42:45], v66, v8, v[42:45]
	v_mfma_f32_4x4x1_16b_f32 v[46:49], v66, v9, v[46:49]
	v_cvt_f32_f16_sdwa v55, v82 dst_sel:DWORD dst_unused:UNUSED_PAD src0_sel:WORD_1
	v_cvt_f32_f16_e32 v54, v82
	v_cvt_f32_f16_sdwa v57, v83 dst_sel:DWORD dst_unused:UNUSED_PAD src0_sel:WORD_1
	v_cvt_f32_f16_e32 v56, v83
	v_cvt_f32_f16_sdwa v59, v84 dst_sel:DWORD dst_unused:UNUSED_PAD src0_sel:WORD_1
	v_cvt_f32_f16_e32 v58, v84
	v_cvt_f32_f16_sdwa v61, v85 dst_sel:DWORD dst_unused:UNUSED_PAD src0_sel:WORD_1
	v_cvt_f32_f16_e32 v60, v85
	v_mfma_f32_4x4x1_16b_f32 v[18:21], v67, v10, v[18:21]
	v_mfma_f32_4x4x1_16b_f32 v[22:25], v67, v11, v[22:25]
	v_mfma_f32_4x4x1_16b_f32 v[26:29], v67, v12, v[26:29]
	v_mfma_f32_4x4x1_16b_f32 v[30:33], v67, v13, v[30:33]
	v_mfma_f32_4x4x1_16b_f32 v[34:37], v67, v14, v[34:37]
	v_mfma_f32_4x4x1_16b_f32 v[38:41], v67, v15, v[38:41]
	v_mfma_f32_4x4x1_16b_f32 v[42:45], v67, v16, v[42:45]
	v_mfma_f32_4x4x1_16b_f32 v[46:49], v67, v17, v[46:49]
	v_mfma_f32_4x4x1_16b_f32 v[18:21], v65, v54, v[18:21]
	v_mfma_f32_4x4x1_16b_f32 v[22:25], v65, v55, v[22:25]
	v_mfma_f32_4x4x1_16b_f32 v[26:29], v65, v56, v[26:29]
	v_mfma_f32_4x4x1_16b_f32 v[30:33], v65, v57, v[30:33]
	v_mfma_f32_4x4x1_16b_f32 v[34:37], v65, v58, v[34:37]
	v_mfma_f32_4x4x1_16b_f32 v[38:41], v65, v59, v[38:41]
	v_mfma_f32_4x4x1_16b_f32 v[42:45], v65, v60, v[42:45]
	v_mfma_f32_4x4x1_16b_f32 v[46:49], v65, v61, v[46:49]
	v_add_u32_e32 v72, 48, v72
	s_add_i32 s2, s2, 3
	ds_read_b32 v66, v72
	ds_read_b32 v67, v72 offset:16
	ds_read_b32 v65, v72 offset:32
	s_waitcnt vmcnt(0)
	v_cvt_f32_f16_sdwa v3, v86 dst_sel:DWORD dst_unused:UNUSED_PAD src0_sel:WORD_1
	v_cvt_f32_f16_e32 v2, v86
	v_cvt_f32_f16_sdwa v5, v87 dst_sel:DWORD dst_unused:UNUSED_PAD src0_sel:WORD_1
	v_cvt_f32_f16_e32 v4, v87
	v_cvt_f32_f16_sdwa v7, v88 dst_sel:DWORD dst_unused:UNUSED_PAD src0_sel:WORD_1
	v_cvt_f32_f16_e32 v6, v88
	v_cvt_f32_f16_sdwa v9, v89 dst_sel:DWORD dst_unused:UNUSED_PAD src0_sel:WORD_1
	v_cvt_f32_f16_e32 v8, v89
	v_cvt_f32_f16_sdwa v11, v90 dst_sel:DWORD dst_unused:UNUSED_PAD src0_sel:WORD_1
	v_cvt_f32_f16_e32 v10, v90
	v_cvt_f32_f16_sdwa v13, v91 dst_sel:DWORD dst_unused:UNUSED_PAD src0_sel:WORD_1
	v_cvt_f32_f16_e32 v12, v91
	v_cvt_f32_f16_sdwa v15, v92 dst_sel:DWORD dst_unused:UNUSED_PAD src0_sel:WORD_1
	v_cvt_f32_f16_e32 v14, v92
	v_cvt_f32_f16_sdwa v17, v93 dst_sel:DWORD dst_unused:UNUSED_PAD src0_sel:WORD_1
	v_cvt_f32_f16_e32 v16, v93
	s_waitcnt lgkmcnt(0)
	v_mfma_f32_4x4x1_16b_f32 v[18:21], v66, v2, v[18:21]
	v_mfma_f32_4x4x1_16b_f32 v[22:25], v66, v3, v[22:25]
	v_mfma_f32_4x4x1_16b_f32 v[26:29], v66, v4, v[26:29]
	v_mfma_f32_4x4x1_16b_f32 v[30:33], v66, v5, v[30:33]
	v_mfma_f32_4x4x1_16b_f32 v[34:37], v66, v6, v[34:37]
	v_mfma_f32_4x4x1_16b_f32 v[38:41], v66, v7, v[38:41]
	v_mfma_f32_4x4x1_16b_f32 v[42:45], v66, v8, v[42:45]
	v_mfma_f32_4x4x1_16b_f32 v[46:49], v66, v9, v[46:49]
	v_cvt_f32_f16_sdwa v55, v50 dst_sel:DWORD dst_unused:UNUSED_PAD src0_sel:WORD_1
	v_cvt_f32_f16_e32 v54, v50
	v_cvt_f32_f16_sdwa v57, v51 dst_sel:DWORD dst_unused:UNUSED_PAD src0_sel:WORD_1
	v_cvt_f32_f16_e32 v56, v51
	v_cvt_f32_f16_sdwa v59, v52 dst_sel:DWORD dst_unused:UNUSED_PAD src0_sel:WORD_1
	v_cvt_f32_f16_e32 v58, v52
	v_cvt_f32_f16_sdwa v61, v53 dst_sel:DWORD dst_unused:UNUSED_PAD src0_sel:WORD_1
	v_cvt_f32_f16_e32 v60, v53
	v_mfma_f32_4x4x1_16b_f32 v[18:21], v67, v10, v[18:21]
	v_mfma_f32_4x4x1_16b_f32 v[22:25], v67, v11, v[22:25]
	v_mfma_f32_4x4x1_16b_f32 v[26:29], v67, v12, v[26:29]
	v_mfma_f32_4x4x1_16b_f32 v[30:33], v67, v13, v[30:33]
	v_mfma_f32_4x4x1_16b_f32 v[34:37], v67, v14, v[34:37]
	v_mfma_f32_4x4x1_16b_f32 v[38:41], v67, v15, v[38:41]
	v_mfma_f32_4x4x1_16b_f32 v[42:45], v67, v16, v[42:45]
	v_mfma_f32_4x4x1_16b_f32 v[46:49], v67, v17, v[46:49]
	v_mfma_f32_4x4x1_16b_f32 v[18:21], v65, v54, v[18:21]
	v_mfma_f32_4x4x1_16b_f32 v[22:25], v65, v55, v[22:25]
	v_mfma_f32_4x4x1_16b_f32 v[26:29], v65, v56, v[26:29]
	v_mfma_f32_4x4x1_16b_f32 v[30:33], v65, v57, v[30:33]
	v_mfma_f32_4x4x1_16b_f32 v[34:37], v65, v58, v[34:37]
	v_mfma_f32_4x4x1_16b_f32 v[38:41], v65, v59, v[38:41]
	v_mfma_f32_4x4x1_16b_f32 v[42:45], v65, v60, v[42:45]
	v_mfma_f32_4x4x1_16b_f32 v[46:49], v65, v61, v[46:49]
	s_branch .Ll1g_done
.Ll1g_lastE:
	ds_read_b32 v66, v72
	ds_read_b32 v67, v72 offset:16
	ds_read_b32 v65, v72 offset:32
	s_waitcnt vmcnt(0)
	v_cvt_f32_f16_sdwa v3, v74 dst_sel:DWORD dst_unused:UNUSED_PAD src0_sel:WORD_1
	v_cvt_f32_f16_e32 v2, v74
	v_cvt_f32_f16_sdwa v5, v75 dst_sel:DWORD dst_unused:UNUSED_PAD src0_sel:WORD_1
	v_cvt_f32_f16_e32 v4, v75
	v_cvt_f32_f16_sdwa v7, v76 dst_sel:DWORD dst_unused:UNUSED_PAD src0_sel:WORD_1
	v_cvt_f32_f16_e32 v6, v76
	v_cvt_f32_f16_sdwa v9, v77 dst_sel:DWORD dst_unused:UNUSED_PAD src0_sel:WORD_1
	v_cvt_f32_f16_e32 v8, v77
	v_cvt_f32_f16_sdwa v11, v78 dst_sel:DWORD dst_unused:UNUSED_PAD src0_sel:WORD_1
	v_cvt_f32_f16_e32 v10, v78
	v_cvt_f32_f16_sdwa v13, v79 dst_sel:DWORD dst_unused:UNUSED_PAD src0_sel:WORD_1
	v_cvt_f32_f16_e32 v12, v79
	v_cvt_f32_f16_sdwa v15, v80 dst_sel:DWORD dst_unused:UNUSED_PAD src0_sel:WORD_1
	v_cvt_f32_f16_e32 v14, v80
	v_cvt_f32_f16_sdwa v17, v81 dst_sel:DWORD dst_unused:UNUSED_PAD src0_sel:WORD_1
	v_cvt_f32_f16_e32 v16, v81
	s_waitcnt lgkmcnt(0)
	v_mfma_f32_4x4x1_16b_f32 v[18:21], v66, v2, v[18:21]
	v_mfma_f32_4x4x1_16b_f32 v[22:25], v66, v3, v[22:25]
	v_mfma_f32_4x4x1_16b_f32 v[26:29], v66, v4, v[26:29]
	v_mfma_f32_4x4x1_16b_f32 v[30:33], v66, v5, v[30:33]
	v_mfma_f32_4x4x1_16b_f32 v[34:37], v66, v6, v[34:37]
	v_mfma_f32_4x4x1_16b_f32 v[38:41], v66, v7, v[38:41]
	v_mfma_f32_4x4x1_16b_f32 v[42:45], v66, v8, v[42:45]
	v_mfma_f32_4x4x1_16b_f32 v[46:49], v66, v9, v[46:49]
	v_cvt_f32_f16_sdwa v55, v82 dst_sel:DWORD dst_unused:UNUSED_PAD src0_sel:WORD_1
	v_cvt_f32_f16_e32 v54, v82
	v_cvt_f32_f16_sdwa v57, v83 dst_sel:DWORD dst_unused:UNUSED_PAD src0_sel:WORD_1
	v_cvt_f32_f16_e32 v56, v83
	v_cvt_f32_f16_sdwa v59, v84 dst_sel:DWORD dst_unused:UNUSED_PAD src0_sel:WORD_1
	v_cvt_f32_f16_e32 v58, v84
	v_cvt_f32_f16_sdwa v61, v85 dst_sel:DWORD dst_unused:UNUSED_PAD src0_sel:WORD_1
	v_cvt_f32_f16_e32 v60, v85
	v_mfma_f32_4x4x1_16b_f32 v[18:21], v67, v10, v[18:21]
	v_mfma_f32_4x4x1_16b_f32 v[22:25], v67, v11, v[22:25]
	v_mfma_f32_4x4x1_16b_f32 v[26:29], v67, v12, v[26:29]
	v_mfma_f32_4x4x1_16b_f32 v[30:33], v67, v13, v[30:33]
	v_mfma_f32_4x4x1_16b_f32 v[34:37], v67, v14, v[34:37]
	v_mfma_f32_4x4x1_16b_f32 v[38:41], v67, v15, v[38:41]
	v_mfma_f32_4x4x1_16b_f32 v[42:45], v67, v16, v[42:45]
	v_mfma_f32_4x4x1_16b_f32 v[46:49], v67, v17, v[46:49]
	v_mfma_f32_4x4x1_16b_f32 v[18:21], v65, v54, v[18:21]
	v_mfma_f32_4x4x1_16b_f32 v[22:25], v65, v55, v[22:25]
	v_mfma_f32_4x4x1_16b_f32 v[26:29], v65, v56, v[26:29]
	v_mfma_f32_4x4x1_16b_f32 v[30:33], v65, v57, v[30:33]
	v_mfma_f32_4x4x1_16b_f32 v[34:37], v65, v58, v[34:37]
	v_mfma_f32_4x4x1_16b_f32 v[38:41], v65, v59, v[38:41]
	v_mfma_f32_4x4x1_16b_f32 v[42:45], v65, v60, v[42:45]
	v_mfma_f32_4x4x1_16b_f32 v[46:49], v65, v61, v[46:49]
	s_branch .Ll1g_done
.Ll1g_tailO:
	s_add_i32 s5, s2, 3
	s_cmp_ge_i32 s5, s3
	s_cbranch_scc1 .Ll1g_lastO
	ds_read_b32 v66, v72
	ds_read_b32 v67, v72 offset:16
	ds_read_b32 v65, v72 offset:32
	s_waitcnt vmcnt(3)
	v_cvt_f32_f16_sdwa v3, v86 dst_sel:DWORD dst_unused:UNUSED_PAD src0_sel:WORD_1
	v_cvt_f32_f16_e32 v2, v86
	v_cvt_f32_f16_sdwa v5, v87 dst_sel:DWORD dst_unused:UNUSED_PAD src0_sel:WORD_1
	v_cvt_f32_f16_e32 v4, v87
	v_cvt_f32_f16_sdwa v7, v88 dst_sel:DWORD dst_unused:UNUSED_PAD src0_sel:WORD_1
	v_cvt_f32_f16_e32 v6, v88
	v_cvt_f32_f16_sdwa v9, v89 dst_sel:DWORD dst_unused:UNUSED_PAD src0_sel:WORD_1
	v_cvt_f32_f16_e32 v8, v89
	v_cvt_f32_f16_sdwa v11, v90 dst_sel:DWORD dst_unused:UNUSED_PAD src0_sel:WORD_1
	v_cvt_f32_f16_e32 v10, v90
	v_cvt_f32_f16_sdwa v13, v91 dst_sel:DWORD dst_unused:UNUSED_PAD src0_sel:WORD_1
	v_cvt_f32_f16_e32 v12, v91
	v_cvt_f32_f16_sdwa v15, v92 dst_sel:DWORD dst_unused:UNUSED_PAD src0_sel:WORD_1
	v_cvt_f32_f16_e32 v14, v92
	v_cvt_f32_f16_sdwa v17, v93 dst_sel:DWORD dst_unused:UNUSED_PAD src0_sel:WORD_1
	v_cvt_f32_f16_e32 v16, v93
	s_waitcnt lgkmcnt(0)
	v_mfma_f32_4x4x1_16b_f32 v[18:21], v66, v2, v[18:21]
	v_mfma_f32_4x4x1_16b_f32 v[22:25], v66, v3, v[22:25]
	v_mfma_f32_4x4x1_16b_f32 v[26:29], v66, v4, v[26:29]
	v_mfma_f32_4x4x1_16b_f32 v[30:33], v66, v5, v[30:33]
	v_mfma_f32_4x4x1_16b_f32 v[34:37], v66, v6, v[34:37]
	v_mfma_f32_4x4x1_16b_f32 v[38:41], v66, v7, v[38:41]
	v_mfma_f32_4x4x1_16b_f32 v[42:45], v66, v8, v[42:45]
	v_mfma_f32_4x4x1_16b_f32 v[46:49], v66, v9, v[46:49]
	v_cvt_f32_f16_sdwa v55, v50 dst_sel:DWORD dst_unused:UNUSED_PAD src0_sel:WORD_1
	v_cvt_f32_f16_e32 v54, v50
	v_cvt_f32_f16_sdwa v57, v51 dst_sel:DWORD dst_unused:UNUSED_PAD src0_sel:WORD_1
	v_cvt_f32_f16_e32 v56, v51
	v_cvt_f32_f16_sdwa v59, v52 dst_sel:DWORD dst_unused:UNUSED_PAD src0_sel:WORD_1
	v_cvt_f32_f16_e32 v58, v52
	v_cvt_f32_f16_sdwa v61, v53 dst_sel:DWORD dst_unused:UNUSED_PAD src0_sel:WORD_1
	v_cvt_f32_f16_e32 v60, v53
	v_mfma_f32_4x4x1_16b_f32 v[18:21], v67, v10, v[18:21]
	v_mfma_f32_4x4x1_16b_f32 v[22:25], v67, v11, v[22:25]
	v_mfma_f32_4x4x1_16b_f32 v[26:29], v67, v12, v[26:29]
	v_mfma_f32_4x4x1_16b_f32 v[30:33], v67, v13, v[30:33]
	v_mfma_f32_4x4x1_16b_f32 v[34:37], v67, v14, v[34:37]
	v_mfma_f32_4x4x1_16b_f32 v[38:41], v67, v15, v[38:41]
	v_mfma_f32_4x4x1_16b_f32 v[42:45], v67, v16, v[42:45]
	v_mfma_f32_4x4x1_16b_f32 v[46:49], v67, v17, v[46:49]
	v_mfma_f32_4x4x1_16b_f32 v[18:21], v65, v54, v[18:21]
	v_mfma_f32_4x4x1_16b_f32 v[22:25], v65, v55, v[22:25]
	v_mfma_f32_4x4x1_16b_f32 v[26:29], v65, v56, v[26:29]
	v_mfma_f32_4x4x1_16b_f32 v[30:33], v65, v57, v[30:33]
	v_mfma_f32_4x4x1_16b_f32 v[34:37], v65, v58, v[34:37]
	v_mfma_f32_4x4x1_16b_f32 v[38:41], v65, v59, v[38:41]
	v_mfma_f32_4x4x1_16b_f32 v[42:45], v65, v60, v[42:45]
	v_mfma_f32_4x4x1_16b_f32 v[46:49], v65, v61, v[46:49]
	v_add_u32_e32 v72, 48, v72
	s_add_i32 s2, s2, 3
	ds_read_b32 v66, v72
	ds_read_b32 v67, v72 offset:16
	ds_read_b32 v65, v72 offset:32
	s_waitcnt vmcnt(0)
	v_cvt_f32_f16_sdwa v3, v74 dst_sel:DWORD dst_unused:UNUSED_PAD src0_sel:WORD_1
	v_cvt_f32_f16_e32 v2, v74
	v_cvt_f32_f16_sdwa v5, v75 dst_sel:DWORD dst_unused:UNUSED_PAD src0_sel:WORD_1
	v_cvt_f32_f16_e32 v4, v75
	v_cvt_f32_f16_sdwa v7, v76 dst_sel:DWORD dst_unused:UNUSED_PAD src0_sel:WORD_1
	v_cvt_f32_f16_e32 v6, v76
	v_cvt_f32_f16_sdwa v9, v77 dst_sel:DWORD dst_unused:UNUSED_PAD src0_sel:WORD_1
	v_cvt_f32_f16_e32 v8, v77
	v_cvt_f32_f16_sdwa v11, v78 dst_sel:DWORD dst_unused:UNUSED_PAD src0_sel:WORD_1
	v_cvt_f32_f16_e32 v10, v78
	v_cvt_f32_f16_sdwa v13, v79 dst_sel:DWORD dst_unused:UNUSED_PAD src0_sel:WORD_1
	v_cvt_f32_f16_e32 v12, v79
	v_cvt_f32_f16_sdwa v15, v80 dst_sel:DWORD dst_unused:UNUSED_PAD src0_sel:WORD_1
	v_cvt_f32_f16_e32 v14, v80
	v_cvt_f32_f16_sdwa v17, v81 dst_sel:DWORD dst_unused:UNUSED_PAD src0_sel:WORD_1
	v_cvt_f32_f16_e32 v16, v81
	s_waitcnt lgkmcnt(0)
	v_mfma_f32_4x4x1_16b_f32 v[18:21], v66, v2, v[18:21]
	v_mfma_f32_4x4x1_16b_f32 v[22:25], v66, v3, v[22:25]
	v_mfma_f32_4x4x1_16b_f32 v[26:29], v66, v4, v[26:29]
	v_mfma_f32_4x4x1_16b_f32 v[30:33], v66, v5, v[30:33]
	v_mfma_f32_4x4x1_16b_f32 v[34:37], v66, v6, v[34:37]
	v_mfma_f32_4x4x1_16b_f32 v[38:41], v66, v7, v[38:41]
	v_mfma_f32_4x4x1_16b_f32 v[42:45], v66, v8, v[42:45]
	v_mfma_f32_4x4x1_16b_f32 v[46:49], v66, v9, v[46:49]
	v_cvt_f32_f16_sdwa v55, v82 dst_sel:DWORD dst_unused:UNUSED_PAD src0_sel:WORD_1
	v_cvt_f32_f16_e32 v54, v82
	v_cvt_f32_f16_sdwa v57, v83 dst_sel:DWORD dst_unused:UNUSED_PAD src0_sel:WORD_1
	v_cvt_f32_f16_e32 v56, v83
	v_cvt_f32_f16_sdwa v59, v84 dst_sel:DWORD dst_unused:UNUSED_PAD src0_sel:WORD_1
	v_cvt_f32_f16_e32 v58, v84
	v_cvt_f32_f16_sdwa v61, v85 dst_sel:DWORD dst_unused:UNUSED_PAD src0_sel:WORD_1
	v_cvt_f32_f16_e32 v60, v85
	v_mfma_f32_4x4x1_16b_f32 v[18:21], v67, v10, v[18:21]
	v_mfma_f32_4x4x1_16b_f32 v[22:25], v67, v11, v[22:25]
	v_mfma_f32_4x4x1_16b_f32 v[26:29], v67, v12, v[26:29]
	v_mfma_f32_4x4x1_16b_f32 v[30:33], v67, v13, v[30:33]
	v_mfma_f32_4x4x1_16b_f32 v[34:37], v67, v14, v[34:37]
	v_mfma_f32_4x4x1_16b_f32 v[38:41], v67, v15, v[38:41]
	v_mfma_f32_4x4x1_16b_f32 v[42:45], v67, v16, v[42:45]
	v_mfma_f32_4x4x1_16b_f32 v[46:49], v67, v17, v[46:49]
	v_mfma_f32_4x4x1_16b_f32 v[18:21], v65, v54, v[18:21]
	v_mfma_f32_4x4x1_16b_f32 v[22:25], v65, v55, v[22:25]
	v_mfma_f32_4x4x1_16b_f32 v[26:29], v65, v56, v[26:29]
	v_mfma_f32_4x4x1_16b_f32 v[30:33], v65, v57, v[30:33]
	v_mfma_f32_4x4x1_16b_f32 v[34:37], v65, v58, v[34:37]
	v_mfma_f32_4x4x1_16b_f32 v[38:41], v65, v59, v[38:41]
	v_mfma_f32_4x4x1_16b_f32 v[42:45], v65, v60, v[42:45]
	v_mfma_f32_4x4x1_16b_f32 v[46:49], v65, v61, v[46:49]
	s_branch .Ll1g_done
.Ll1g_lastO:
	ds_read_b32 v66, v72
	ds_read_b32 v67, v72 offset:16
	ds_read_b32 v65, v72 offset:32
	s_waitcnt vmcnt(0)
	v_cvt_f32_f16_sdwa v3, v86 dst_sel:DWORD dst_unused:UNUSED_PAD src0_sel:WORD_1
	v_cvt_f32_f16_e32 v2, v86
	v_cvt_f32_f16_sdwa v5, v87 dst_sel:DWORD dst_unused:UNUSED_PAD src0_sel:WORD_1
	v_cvt_f32_f16_e32 v4, v87
	v_cvt_f32_f16_sdwa v7, v88 dst_sel:DWORD dst_unused:UNUSED_PAD src0_sel:WORD_1
	v_cvt_f32_f16_e32 v6, v88
	v_cvt_f32_f16_sdwa v9, v89 dst_sel:DWORD dst_unused:UNUSED_PAD src0_sel:WORD_1
	v_cvt_f32_f16_e32 v8, v89
	v_cvt_f32_f16_sdwa v11, v90 dst_sel:DWORD dst_unused:UNUSED_PAD src0_sel:WORD_1
	v_cvt_f32_f16_e32 v10, v90
	v_cvt_f32_f16_sdwa v13, v91 dst_sel:DWORD dst_unused:UNUSED_PAD src0_sel:WORD_1
	v_cvt_f32_f16_e32 v12, v91
	v_cvt_f32_f16_sdwa v15, v92 dst_sel:DWORD dst_unused:UNUSED_PAD src0_sel:WORD_1
	v_cvt_f32_f16_e32 v14, v92
	v_cvt_f32_f16_sdwa v17, v93 dst_sel:DWORD dst_unused:UNUSED_PAD src0_sel:WORD_1
	v_cvt_f32_f16_e32 v16, v93
	s_waitcnt lgkmcnt(0)
	v_mfma_f32_4x4x1_16b_f32 v[18:21], v66, v2, v[18:21]
	v_mfma_f32_4x4x1_16b_f32 v[22:25], v66, v3, v[22:25]
	v_mfma_f32_4x4x1_16b_f32 v[26:29], v66, v4, v[26:29]
	v_mfma_f32_4x4x1_16b_f32 v[30:33], v66, v5, v[30:33]
	v_mfma_f32_4x4x1_16b_f32 v[34:37], v66, v6, v[34:37]
	v_mfma_f32_4x4x1_16b_f32 v[38:41], v66, v7, v[38:41]
	v_mfma_f32_4x4x1_16b_f32 v[42:45], v66, v8, v[42:45]
	v_mfma_f32_4x4x1_16b_f32 v[46:49], v66, v9, v[46:49]
	v_cvt_f32_f16_sdwa v55, v50 dst_sel:DWORD dst_unused:UNUSED_PAD src0_sel:WORD_1
	v_cvt_f32_f16_e32 v54, v50
	v_cvt_f32_f16_sdwa v57, v51 dst_sel:DWORD dst_unused:UNUSED_PAD src0_sel:WORD_1
	v_cvt_f32_f16_e32 v56, v51
	v_cvt_f32_f16_sdwa v59, v52 dst_sel:DWORD dst_unused:UNUSED_PAD src0_sel:WORD_1
	v_cvt_f32_f16_e32 v58, v52
	v_cvt_f32_f16_sdwa v61, v53 dst_sel:DWORD dst_unused:UNUSED_PAD src0_sel:WORD_1
	v_cvt_f32_f16_e32 v60, v53
	v_mfma_f32_4x4x1_16b_f32 v[18:21], v67, v10, v[18:21]
	v_mfma_f32_4x4x1_16b_f32 v[22:25], v67, v11, v[22:25]
	v_mfma_f32_4x4x1_16b_f32 v[26:29], v67, v12, v[26:29]
	v_mfma_f32_4x4x1_16b_f32 v[30:33], v67, v13, v[30:33]
	v_mfma_f32_4x4x1_16b_f32 v[34:37], v67, v14, v[34:37]
	v_mfma_f32_4x4x1_16b_f32 v[38:41], v67, v15, v[38:41]
	v_mfma_f32_4x4x1_16b_f32 v[42:45], v67, v16, v[42:45]
	v_mfma_f32_4x4x1_16b_f32 v[46:49], v67, v17, v[46:49]
	v_mfma_f32_4x4x1_16b_f32 v[18:21], v65, v54, v[18:21]
	v_mfma_f32_4x4x1_16b_f32 v[22:25], v65, v55, v[22:25]
	v_mfma_f32_4x4x1_16b_f32 v[26:29], v65, v56, v[26:29]
	v_mfma_f32_4x4x1_16b_f32 v[30:33], v65, v57, v[30:33]
	v_mfma_f32_4x4x1_16b_f32 v[34:37], v65, v58, v[34:37]
	v_mfma_f32_4x4x1_16b_f32 v[38:41], v65, v59, v[38:41]
	v_mfma_f32_4x4x1_16b_f32 v[42:45], v65, v60, v[42:45]
	v_mfma_f32_4x4x1_16b_f32 v[46:49], v65, v61, v[46:49]
.Ll1g_done:
	s_setprio 0
	v_add_u32_e32 v6, v70, v71
	s_nop 4
	v_cvt_pk_f16_f32 v2, v18, v22
	v_cvt_pk_f16_f32 v3, v26, v30
	v_cvt_pk_f16_f32 v4, v34, v38
	v_cvt_pk_f16_f32 v5, v42, v46
	ds_write_b128 v6, v[2:5]
	v_cvt_pk_f16_f32 v2, v19, v23
	v_cvt_pk_f16_f32 v3, v27, v31
	v_cvt_pk_f16_f32 v4, v35, v39
	v_cvt_pk_f16_f32 v5, v43, v47
	ds_write_b128 v6, v[2:5] offset:256
	v_cvt_pk_f16_f32 v2, v20, v24
	v_cvt_pk_f16_f32 v3, v28, v32
	v_cvt_pk_f16_f32 v4, v36, v40
	v_cvt_pk_f16_f32 v5, v44, v48
	ds_write_b128 v6, v[2:5] offset:512
	v_cvt_pk_f16_f32 v2, v21, v25
	v_cvt_pk_f16_f32 v3, v29, v33
	v_cvt_pk_f16_f32 v4, v37, v41
	v_cvt_pk_f16_f32 v5, v45, v49
	ds_write_b128 v6, v[2:5] offset:768
